# speedup vs baseline: 1.0090x; 1.0090x over previous
.LBB2_29:
	v_cmp_lt_u32_sdwa s[0:1], v19, v8 src0_sel:DWORD src1_sel:WORD_1
	v_add_u32_e32 v42, 8, v19
	v_cmp_lt_u32_sdwa s[30:31], v42, v8 src0_sel:DWORD src1_sel:WORD_1
	v_cndmask_b32_e64 v2, 0, v19, s[0:1]
	v_add_u32_e32 v2, v2, v20
	v_lshl_add_u64 v[26:27], v[2:3], 2, s[60:61]
	v_cndmask_b32_e64 v2, 0, v42, s[30:31]
	v_add_u32_e32 v43, 16, v19
	v_add_u32_e32 v2, v2, v20
	v_cmp_lt_u32_sdwa s[4:5], v43, v8 src0_sel:DWORD src1_sel:WORD_1
	v_lshl_add_u64 v[28:29], v[2:3], 2, s[60:61]
	v_cmp_lt_u32_sdwa s[6:7], v19, v9 src0_sel:DWORD src1_sel:WORD_1
	v_cndmask_b32_e64 v2, 0, v43, s[4:5]
	v_add_u32_e32 v2, v2, v20
	v_lshl_add_u64 v[30:31], v[2:3], 2, s[60:61]
	v_cndmask_b32_e64 v2, 0, v19, s[6:7]
	v_add_u32_e32 v2, v2, v21
	v_cmp_lt_u32_sdwa s[8:9], v42, v9 src0_sel:DWORD src1_sel:WORD_1
	v_lshl_add_u64 v[32:33], v[2:3], 2, s[60:61]
	v_cmp_lt_u32_sdwa s[10:11], v43, v9 src0_sel:DWORD src1_sel:WORD_1
	v_cndmask_b32_e64 v2, 0, v42, s[8:9]
	v_add_u32_e32 v2, v2, v21
	v_lshl_add_u64 v[34:35], v[2:3], 2, s[60:61]
	v_cndmask_b32_e64 v2, 0, v43, s[10:11]
	v_add_u32_e32 v2, v2, v21
	v_cmp_lt_u32_e64 s[12:13], v19, v7
	v_lshl_add_u64 v[36:37], v[2:3], 2, s[60:61]
	v_cmp_lt_u32_e64 s[14:15], v42, v7
	v_cndmask_b32_e64 v2, 0, v19, s[12:13]
	v_add_u32_e32 v2, v2, v22
	v_lshl_add_u64 v[38:39], v[2:3], 2, s[60:61]
	v_cndmask_b32_e64 v2, 0, v42, s[14:15]
	v_add_u32_e32 v2, v2, v22
	v_cmp_lt_u32_e64 s[16:17], v43, v7
	v_lshl_add_u64 v[40:41], v[2:3], 2, s[60:61]
	v_cmp_lt_u32_e64 s[18:19], v19, v13
	v_cndmask_b32_e64 v2, 0, v43, s[16:17]
	v_add_u32_e32 v2, v2, v22
	global_load_dword v44, v[26:27], off
	global_load_dword v45, v[28:29], off
	global_load_dword v46, v[30:31], off
	global_load_dword v47, v[32:33], off
	s_waitcnt lgkmcnt(5)
	global_load_dword v49, v[34:35], off
	s_waitcnt lgkmcnt(4)
	global_load_dword v50, v[36:37], off
	global_load_dword v51, v[38:39], off
	global_load_dword v52, v[40:41], off
	v_lshl_add_u64 v[26:27], v[2:3], 2, s[60:61]
	v_cndmask_b32_e64 v2, 0, v19, s[18:19]
	v_add_u32_e32 v2, v2, v23
	v_cmp_lt_u32_e64 s[20:21], v42, v13
	v_lshl_add_u64 v[28:29], v[2:3], 2, s[60:61]
	v_cmp_lt_u32_e64 s[22:23], v43, v13
	v_cndmask_b32_e64 v2, 0, v42, s[20:21]
	v_add_u32_e32 v2, v2, v23
	v_lshl_add_u64 v[30:31], v[2:3], 2, s[60:61]
	v_cndmask_b32_e64 v2, 0, v43, s[22:23]
	v_add_u32_e32 v2, v2, v23
	v_cmp_lt_u32_e64 s[24:25], v19, v14
	v_lshl_add_u64 v[32:33], v[2:3], 2, s[60:61]
	v_cmp_lt_u32_e64 s[26:27], v42, v14
	v_cndmask_b32_e64 v2, 0, v19, s[24:25]
	v_add_u32_e32 v2, v2, v4
	v_lshl_add_u64 v[34:35], v[2:3], 2, s[60:61]
	v_cndmask_b32_e64 v2, 0, v42, s[26:27]
	v_add_u32_e32 v2, v2, v4
	v_cmp_lt_u32_e64 s[28:29], v43, v14
	v_lshl_add_u64 v[36:37], v[2:3], 2, s[60:61]
	v_cmp_lt_u32_e64 s[34:35], v19, v15
	v_cndmask_b32_e64 v2, 0, v43, s[28:29]
	v_add_u32_e32 v2, v2, v4
	v_lshl_add_u64 v[38:39], v[2:3], 2, s[60:61]
	v_cndmask_b32_e64 v2, 0, v19, s[34:35]
	v_add_u32_e32 v2, v2, v5
	v_cmp_lt_u32_e64 s[36:37], v42, v15
	v_lshl_add_u64 v[40:41], v[2:3], 2, s[60:61]
	v_cmp_lt_u32_e64 s[38:39], v43, v15
	v_cndmask_b32_e64 v2, 0, v42, s[36:37]
	v_add_u32_e32 v2, v2, v5
	s_waitcnt lgkmcnt(1)
	global_load_dword v53, v[26:27], off
	global_load_dword v54, v[28:29], off
	s_waitcnt lgkmcnt(0)
	global_load_dword v55, v[30:31], off
	global_load_dword v56, v[32:33], off
	global_load_dword v57, v[34:35], off
	global_load_dword v58, v[36:37], off
	global_load_dword v59, v[38:39], off
	global_load_dword v60, v[40:41], off
	v_lshl_add_u64 v[26:27], v[2:3], 2, s[60:61]
	v_cndmask_b32_e64 v2, 0, v43, s[38:39]
	v_add_u32_e32 v2, v2, v5
	v_cmp_lt_u32_e64 s[40:41], v19, v16
	v_lshl_add_u64 v[28:29], v[2:3], 2, s[60:61]
	v_cmp_lt_u32_e64 s[42:43], v42, v16
	v_cndmask_b32_e64 v2, 0, v19, s[40:41]
	v_add_u32_e32 v2, v2, v10
	v_lshl_add_u64 v[30:31], v[2:3], 2, s[60:61]
	v_cndmask_b32_e64 v2, 0, v42, s[42:43]
	v_add_u32_e32 v2, v2, v10
	v_cmp_lt_u32_e64 s[44:45], v43, v16
	v_lshl_add_u64 v[32:33], v[2:3], 2, s[60:61]
	v_cmp_lt_u32_e64 s[46:47], v19, v17
	v_cndmask_b32_e64 v2, 0, v43, s[44:45]
	v_add_u32_e32 v2, v2, v10
	v_lshl_add_u64 v[34:35], v[2:3], 2, s[60:61]
	v_cndmask_b32_e64 v2, 0, v19, s[46:47]
	v_add_u32_e32 v2, v2, v11
	v_cmp_lt_u32_e64 s[48:49], v42, v17
	v_lshl_add_u64 v[36:37], v[2:3], 2, s[60:61]
	v_cmp_lt_u32_e64 s[50:51], v43, v17
	v_cndmask_b32_e64 v2, 0, v42, s[48:49]
	v_add_u32_e32 v2, v2, v11
	v_lshl_add_u64 v[38:39], v[2:3], 2, s[60:61]
	v_cndmask_b32_e64 v2, 0, v43, s[50:51]
	v_add_u32_e32 v2, v2, v11
	v_lshl_add_u64 v[40:41], v[2:3], 2, s[60:61]
	global_load_dword v2, v[26:27], off
	s_nop 0
	global_load_dword v26, v[28:29], off
	global_load_dword v42, v[30:31], off
	s_nop 0
	global_load_dword v33, v[32:33], off
	s_nop 0
	global_load_dword v61, v[34:35], off
	global_load_dword v62, v[36:37], off
	global_load_dword v63, v[38:39], off
	global_load_dword v64, v[40:41], off
	s_waitcnt vmcnt(23)
	v_cndmask_b32_e64 v48, -1, v44, s[0:1]
	s_waitcnt vmcnt(22)
	v_cndmask_b32_e64 v40, -1, v45, s[30:31]
	s_waitcnt vmcnt(21)
	v_cndmask_b32_e64 v32, -1, v46, s[4:5]
	s_waitcnt vmcnt(20)
	v_cndmask_b32_e64 v47, -1, v47, s[6:7]
	s_waitcnt vmcnt(19)
	v_cndmask_b32_e64 v39, -1, v49, s[8:9]
	s_waitcnt vmcnt(18)
	v_cndmask_b32_e64 v31, -1, v50, s[10:11]
	v_and_b32_e32 v50, 0xffff, v47
	s_waitcnt vmcnt(17)
	v_cndmask_b32_e64 v46, -1, v51, s[12:13]
	s_waitcnt vmcnt(16)
	v_cndmask_b32_e64 v38, -1, v52, s[14:15]
	v_cmp_eq_u32_e64 s[0:1], -1, v46
	v_cmp_eq_u32_e64 s[12:13], -1, v40
	v_cmp_eq_u32_e64 s[14:15], -1, v39
	v_and_b32_e32 v49, 0xffff, v48
	v_bfe_u32 v70, v48, 16, 7
	s_waitcnt vmcnt(15)
	v_cndmask_b32_e64 v30, -1, v53, s[16:17]
	s_waitcnt vmcnt(14)
	v_cndmask_b32_e64 v45, -1, v54, s[18:19]
	v_cmp_eq_u32_e64 s[18:19], -1, v47
	s_waitcnt vmcnt(12)
	v_cndmask_b32_e64 v29, -1, v56, s[22:23]
	s_waitcnt vmcnt(11)
	v_cndmask_b32_e64 v44, -1, v57, s[24:25]
	v_cndmask_b32_e64 v50, v50, 0, s[18:19]
	v_lshlrev_b32_e32 v52, 3, v50
	v_and_b32_e32 v50, 0xffff, v46
	v_cndmask_b32_e64 v50, v50, 0, s[0:1]
	v_lshlrev_b32_e32 v54, 3, v50
	v_and_b32_e32 v50, 0xffff, v45
	v_cmp_eq_u32_e64 s[4:5], -1, v44
	s_waitcnt vmcnt(8)
	v_cndmask_b32_e64 v43, -1, v60, s[34:35]
	v_cndmask_b32_e64 v36, -1, v58, s[26:27]
	v_cmp_eq_u32_e64 s[6:7], -1, v43
	v_cndmask_b32_e64 v37, -1, v55, s[20:21]
	v_cmp_eq_u32_e64 s[20:21], -1, v48
	v_cndmask_b32_e64 v28, -1, v59, s[28:29]
	v_cmp_eq_u32_e64 s[16:17], -1, v38
	v_cndmask_b32_e64 v49, v49, 0, s[20:21]
	v_and_b32_e32 v55, 0xffff, v36
	v_cmp_eq_u32_e64 s[34:35], -1, v30
	v_lshlrev_b32_e32 v49, 3, v49
	v_and_b32_e32 v65, 0xffff, v29
	v_cmp_eq_u32_e64 s[30:31], -1, v29
	v_cmp_eq_u32_e64 s[28:29], -1, v28
	v_cndmask_b32_e64 v70, v70, v24, s[20:21]
	v_cndmask_b32_e64 v65, v65, 0, s[30:31]
	v_lshlrev_b32_e32 v81, 3, v65
	s_waitcnt vmcnt(7)
	v_cndmask_b32_e64 v35, -1, v2, s[36:37]
	s_waitcnt vmcnt(6)
	v_cndmask_b32_e64 v27, -1, v26, s[38:39]
	s_waitcnt vmcnt(5)
	v_cndmask_b32_e64 v42, -1, v42, s[40:41]
	v_cmp_eq_u32_e64 s[8:9], -1, v42
	s_waitcnt vmcnt(4)
	v_cndmask_b32_e64 v34, -1, v33, s[42:43]
	s_waitcnt vmcnt(2)
	v_cndmask_b32_e64 v41, -1, v62, s[46:47]
	v_cmp_eq_u32_e64 s[10:11], -1, v41
	s_waitcnt vmcnt(0)
	v_cndmask_b32_e64 v2, -1, v64, s[50:51]
	v_cmp_eq_u32_e64 s[50:51], -1, v45
	v_cndmask_b32_e64 v33, -1, v63, s[48:49]
	v_cmp_eq_u32_e64 s[46:47], -1, v36
	v_cndmask_b32_e64 v50, v50, 0, s[50:51]
	v_lshlrev_b32_e32 v56, 3, v50
	v_and_b32_e32 v50, 0xffff, v44
	v_cndmask_b32_e64 v50, v50, 0, s[4:5]
	v_lshlrev_b32_e32 v58, 3, v50
	v_and_b32_e32 v50, 0xffff, v43
	v_cndmask_b32_e64 v50, v50, 0, s[6:7]
	v_lshlrev_b32_e32 v60, 3, v50
	v_and_b32_e32 v50, 0xffff, v42
	v_cndmask_b32_e64 v50, v50, 0, s[8:9]
	v_lshlrev_b32_e32 v62, 3, v50
	v_and_b32_e32 v50, 0xffff, v41
	v_cndmask_b32_e64 v50, v50, 0, s[10:11]
	v_lshlrev_b32_e32 v64, 3, v50
	v_and_b32_e32 v50, 0xffff, v40
	v_cndmask_b32_e64 v50, v50, 0, s[12:13]
	v_lshlrev_b32_e32 v66, 3, v50
	v_and_b32_e32 v50, 0xffff, v39
	v_cndmask_b32_e64 v50, v50, 0, s[14:15]
	v_lshlrev_b32_e32 v68, 3, v50
	v_and_b32_e32 v50, 0xffff, v38
	v_and_b32_e32 v59, 0xffff, v33
	v_cmp_eq_u32_e64 s[40:41], -1, v33
	v_and_b32_e32 v63, 0xffff, v30
	v_cndmask_b32_e64 v53, v50, 0, s[16:17]
	v_cndmask_b32_e64 v55, v55, 0, s[46:47]
	v_cndmask_b32_e64 v59, v59, 0, s[40:41]
	v_cndmask_b32_e64 v63, v63, 0, s[34:35]
	global_load_dwordx2 v[50:51], v49, s[58:59]
	v_cmp_eq_u32_e64 s[48:49], -1, v37
	v_lshlrev_b32_e32 v74, 3, v55
	global_load_dwordx2 v[54:55], v54, s[58:59]
	v_lshlrev_b32_e32 v77, 3, v59
	global_load_dwordx2 v[58:59], v58, s[58:59]
	v_lshlrev_b32_e32 v80, 3, v63
	global_load_dwordx2 v[62:63], v62, s[58:59]
	v_lshlrev_b32_e32 v49, 3, v53
	v_and_b32_e32 v53, 0xffff, v37
	v_cndmask_b32_e64 v53, v53, 0, s[48:49]
	v_lshlrev_b32_e32 v72, 3, v53
	global_load_dwordx2 v[52:53], v52, s[58:59]
	v_cndmask_b32_e64 v26, -1, v61, s[44:45]
	v_and_b32_e32 v57, 0xffff, v35
	v_cmp_eq_u32_e64 s[44:45], -1, v35
	v_cmp_eq_u32_e64 s[42:43], -1, v34
	v_and_b32_e32 v61, 0xffff, v32
	v_cndmask_b32_e64 v57, v57, 0, s[44:45]
	v_lshlrev_b32_e32 v75, 3, v57
	v_and_b32_e32 v57, 0xffff, v34
	v_cndmask_b32_e64 v57, v57, 0, s[42:43]
	v_lshlrev_b32_e32 v76, 3, v57
	global_load_dwordx2 v[56:57], v56, s[58:59]
	v_cmp_eq_u32_e64 s[38:39], -1, v32
	v_cmp_eq_u32_e64 s[36:37], -1, v31
	v_and_b32_e32 v65, 0xffff, v28
	v_cndmask_b32_e64 v61, v61, 0, s[38:39]
	v_lshlrev_b32_e32 v78, 3, v61
	v_and_b32_e32 v61, 0xffff, v31
	v_cndmask_b32_e64 v61, v61, 0, s[36:37]
	v_lshlrev_b32_e32 v79, 3, v61
	global_load_dwordx2 v[60:61], v60, s[58:59]
	v_cndmask_b32_e64 v65, v65, 0, s[28:29]
	v_lshlrev_b32_e32 v82, 3, v65
	global_load_dwordx2 v[64:65], v64, s[58:59]
	v_and_b32_e32 v67, 0xffff, v27
	v_cmp_eq_u32_e64 s[26:27], -1, v27
	v_and_b32_e32 v69, 0xffff, v26
	v_cmp_eq_u32_e64 s[24:25], -1, v26
	v_cndmask_b32_e64 v67, v67, 0, s[26:27]
	v_lshlrev_b32_e32 v83, 3, v67
	global_load_dwordx2 v[66:67], v66, s[58:59]
	v_cndmask_b32_e64 v69, v69, 0, s[24:25]
	v_lshlrev_b32_e32 v84, 3, v69
	v_and_b32_e32 v69, 0xffff, v2
	v_cmp_eq_u32_e64 s[22:23], -1, v2
	v_lshlrev_b32_e32 v91, 2, v70
	v_cmp_ne_u32_e64 s[20:21], -1, v35
	v_cndmask_b32_e64 v69, v69, 0, s[22:23]
	v_lshlrev_b32_e32 v85, 3, v69
	global_load_dwordx2 v[68:69], v68, s[58:59]
	s_nop 0
	global_load_dwordx2 v[70:71], v49, s[58:59]
	s_nop 0
	global_load_dwordx2 v[72:73], v72, s[58:59]
	s_nop 0
	global_load_dwordx2 v[98:99], v74, s[58:59]
	global_load_dwordx2 v[100:101], v75, s[58:59]
	global_load_dwordx2 v[102:103], v76, s[58:59]
	global_load_dwordx2 v[104:105], v77, s[58:59]
	global_load_dwordx2 v[106:107], v78, s[58:59]
	global_load_dwordx2 v[108:109], v79, s[58:59]
	global_load_dwordx2 v[110:111], v80, s[58:59]
	global_load_dwordx2 v[112:113], v81, s[58:59]
	global_load_dwordx2 v[114:115], v82, s[58:59]
	global_load_dwordx2 v[116:117], v83, s[58:59]
	global_load_dwordx2 v[118:119], v84, s[58:59]
	global_load_dwordx2 v[120:121], v85, s[58:59]
	v_bfe_u32 v49, v47, 16, 7
	s_waitcnt vmcnt(23)
	ds_add_u32 v91, v50 offset:1024
	ds_add_u32 v91, v51 offset:1792
	v_cndmask_b32_e64 v49, v49, v24, s[18:19]
	v_lshlrev_b32_e32 v49, 2, v49
	ds_add_rtn_u32 v96, v91, v25 offset:2560
	s_waitcnt vmcnt(19)
	s_andn2_b64 s[68:69], exec, s[18:19]
	s_cbranch_scc0 .Lcsk_0
	s_mov_b64 s[70:71], exec
	s_mov_b64 exec, s[68:69]
	ds_add_u32 v49, v52 offset:1024
	ds_add_u32 v49, v53 offset:1792
	ds_add_rtn_u32 v94, v49, v25 offset:2560
	ds_read_b32 v95, v49 offset:3328
	s_mov_b64 exec, s[70:71]
.Lcsk_0:
	v_bfe_u32 v49, v46, 16, 7
	v_cndmask_b32_e64 v49, v49, v24, s[0:1]
	v_lshlrev_b32_e32 v49, 2, v49
	s_andn2_b64 s[68:69], exec, s[0:1]
	s_cbranch_scc0 .Lcsk_1
	s_mov_b64 s[70:71], exec
	s_mov_b64 exec, s[68:69]
	ds_add_u32 v49, v54 offset:1024
	ds_add_u32 v49, v55 offset:1792
	ds_add_rtn_u32 v92, v49, v25 offset:2560
	ds_read_b32 v93, v49 offset:3328
	s_mov_b64 exec, s[70:71]
.Lcsk_1:
	v_bfe_u32 v49, v45, 16, 7
	v_cndmask_b32_e64 v49, v49, v24, s[50:51]
	v_lshlrev_b32_e32 v49, 2, v49
	s_waitcnt vmcnt(18)
	s_andn2_b64 s[68:69], exec, s[50:51]
	s_cbranch_scc0 .Lcsk_2
	s_mov_b64 s[70:71], exec
	s_mov_b64 exec, s[68:69]
	ds_add_u32 v49, v56 offset:1024
	ds_add_u32 v49, v57 offset:1792
	ds_add_rtn_u32 v89, v49, v25 offset:2560
	ds_read_b32 v90, v49 offset:3328
	s_mov_b64 exec, s[70:71]
.Lcsk_2:
	v_bfe_u32 v49, v44, 16, 7
	v_cndmask_b32_e64 v49, v49, v24, s[4:5]
	v_lshlrev_b32_e32 v49, 2, v49
	s_andn2_b64 s[68:69], exec, s[4:5]
	s_cbranch_scc0 .Lcsk_3
	s_mov_b64 s[70:71], exec
	s_mov_b64 exec, s[68:69]
	ds_add_u32 v49, v58 offset:1024
	ds_add_u32 v49, v59 offset:1792
	ds_add_rtn_u32 v87, v49, v25 offset:2560
	ds_read_b32 v88, v49 offset:3328
	s_mov_b64 exec, s[70:71]
.Lcsk_3:
	v_bfe_u32 v49, v43, 16, 7
	v_cndmask_b32_e64 v49, v49, v24, s[6:7]
	v_lshlrev_b32_e32 v49, 2, v49
	s_waitcnt vmcnt(17)
	s_andn2_b64 s[68:69], exec, s[6:7]
	s_cbranch_scc0 .Lcsk_4
	s_mov_b64 s[70:71], exec
	s_mov_b64 exec, s[68:69]
	ds_add_u32 v49, v60 offset:1024
	ds_add_u32 v49, v61 offset:1792
	ds_add_rtn_u32 v85, v49, v25 offset:2560
	ds_read_b32 v86, v49 offset:3328
	s_mov_b64 exec, s[70:71]
.Lcsk_4:
	v_bfe_u32 v49, v42, 16, 7
	v_cndmask_b32_e64 v49, v49, v24, s[8:9]
	v_lshlrev_b32_e32 v49, 2, v49
	s_andn2_b64 s[68:69], exec, s[8:9]
	s_cbranch_scc0 .Lcsk_5
	s_mov_b64 s[70:71], exec
	s_mov_b64 exec, s[68:69]
	ds_add_u32 v49, v62 offset:1024
	ds_add_u32 v49, v63 offset:1792
	ds_add_rtn_u32 v83, v49, v25 offset:2560
	ds_read_b32 v84, v49 offset:3328
	s_mov_b64 exec, s[70:71]
.Lcsk_5:
	v_bfe_u32 v49, v41, 16, 7
	v_cndmask_b32_e64 v49, v49, v24, s[10:11]
	v_lshlrev_b32_e32 v49, 2, v49
	s_waitcnt vmcnt(16)
	s_andn2_b64 s[68:69], exec, s[10:11]
	s_cbranch_scc0 .Lcsk_6
	s_mov_b64 s[70:71], exec
	s_mov_b64 exec, s[68:69]
	ds_add_u32 v49, v64 offset:1024
	ds_add_u32 v49, v65 offset:1792
	ds_add_rtn_u32 v81, v49, v25 offset:2560
	ds_read_b32 v82, v49 offset:3328
	s_mov_b64 exec, s[70:71]
.Lcsk_6:
	v_bfe_u32 v49, v40, 16, 7
	v_cndmask_b32_e64 v49, v49, v24, s[12:13]
	v_lshlrev_b32_e32 v49, 2, v49
	s_waitcnt vmcnt(15)
	s_andn2_b64 s[68:69], exec, s[12:13]
	s_cbranch_scc0 .Lcsk_7
	s_mov_b64 s[70:71], exec
	s_mov_b64 exec, s[68:69]
	ds_add_u32 v49, v66 offset:1024
	ds_add_u32 v49, v67 offset:1792
	ds_add_rtn_u32 v79, v49, v25 offset:2560
	ds_read_b32 v80, v49 offset:3328
	s_mov_b64 exec, s[70:71]
.Lcsk_7:
	v_bfe_u32 v49, v39, 16, 7
	v_cndmask_b32_e64 v49, v49, v24, s[14:15]
	v_lshlrev_b32_e32 v49, 2, v49
	s_waitcnt vmcnt(14)
	s_andn2_b64 s[68:69], exec, s[14:15]
	s_cbranch_scc0 .Lcsk_8
	s_mov_b64 s[70:71], exec
	s_mov_b64 exec, s[68:69]
	ds_add_u32 v49, v68 offset:1024
	ds_add_u32 v49, v69 offset:1792
	ds_add_rtn_u32 v77, v49, v25 offset:2560
	ds_read_b32 v78, v49 offset:3328
	s_mov_b64 exec, s[70:71]
.Lcsk_8:
	v_bfe_u32 v49, v38, 16, 7
	v_cndmask_b32_e64 v49, v49, v24, s[16:17]
	v_lshlrev_b32_e32 v49, 2, v49
	s_waitcnt vmcnt(13)
	s_andn2_b64 s[68:69], exec, s[16:17]
	s_cbranch_scc0 .Lcsk_9
	s_mov_b64 s[70:71], exec
	s_mov_b64 exec, s[68:69]
	ds_add_u32 v49, v70 offset:1024
	ds_add_u32 v49, v71 offset:1792
	ds_add_rtn_u32 v75, v49, v25 offset:2560
	ds_read_b32 v76, v49 offset:3328
	s_mov_b64 exec, s[70:71]
.Lcsk_9:
	v_bfe_u32 v49, v37, 16, 7
	v_cndmask_b32_e64 v49, v49, v24, s[48:49]
	v_lshlrev_b32_e32 v49, 2, v49
	s_waitcnt vmcnt(12)
	s_andn2_b64 s[68:69], exec, s[48:49]
	s_cbranch_scc0 .Lcsk_10
	s_mov_b64 s[70:71], exec
	s_mov_b64 exec, s[68:69]
	ds_add_u32 v49, v72 offset:1024
	ds_add_u32 v49, v73 offset:1792
	ds_add_rtn_u32 v73, v49, v25 offset:2560
	ds_read_b32 v74, v49 offset:3328
	s_mov_b64 exec, s[70:71]
.Lcsk_10:
	v_bfe_u32 v49, v36, 16, 7
	v_cndmask_b32_e64 v49, v49, v24, s[46:47]
	v_lshlrev_b32_e32 v49, 2, v49
	s_waitcnt vmcnt(11)
	s_andn2_b64 s[68:69], exec, s[46:47]
	s_cbranch_scc0 .Lcsk_11
	s_mov_b64 s[70:71], exec
	s_mov_b64 exec, s[68:69]
	ds_add_u32 v49, v98 offset:1024
	ds_add_u32 v49, v99 offset:1792
	ds_add_rtn_u32 v71, v49, v25 offset:2560
	ds_read_b32 v72, v49 offset:3328
	s_mov_b64 exec, s[70:71]
.Lcsk_11:
	v_bfe_u32 v49, v35, 16, 7
	v_cndmask_b32_e64 v49, v49, v24, s[44:45]
	v_lshlrev_b32_e32 v49, 2, v49
	s_waitcnt vmcnt(10)
	s_andn2_b64 s[68:69], exec, s[44:45]
	s_cbranch_scc0 .Lcsk_12
	s_mov_b64 s[70:71], exec
	s_mov_b64 exec, s[68:69]
	ds_add_u32 v49, v100 offset:1024
	ds_add_u32 v49, v101 offset:1792
	ds_add_rtn_u32 v69, v49, v25 offset:2560
	ds_read_b32 v70, v49 offset:3328
	s_mov_b64 exec, s[70:71]
.Lcsk_12:
	v_bfe_u32 v49, v34, 16, 7
	v_cndmask_b32_e64 v49, v49, v24, s[42:43]
	v_lshlrev_b32_e32 v49, 2, v49
	s_waitcnt vmcnt(9)
	s_andn2_b64 s[68:69], exec, s[42:43]
	s_cbranch_scc0 .Lcsk_13
	s_mov_b64 s[70:71], exec
	s_mov_b64 exec, s[68:69]
	ds_add_u32 v49, v102 offset:1024
	ds_add_u32 v49, v103 offset:1792
	ds_add_rtn_u32 v67, v49, v25 offset:2560
	ds_read_b32 v68, v49 offset:3328
	s_mov_b64 exec, s[70:71]
.Lcsk_13:
	v_bfe_u32 v49, v33, 16, 7
	v_cndmask_b32_e64 v49, v49, v24, s[40:41]
	v_lshlrev_b32_e32 v49, 2, v49
	s_waitcnt vmcnt(8)
	s_andn2_b64 s[68:69], exec, s[40:41]
	s_cbranch_scc0 .Lcsk_14
	s_mov_b64 s[70:71], exec
	s_mov_b64 exec, s[68:69]
	ds_add_u32 v49, v104 offset:1024
	ds_add_u32 v49, v105 offset:1792
	ds_add_rtn_u32 v65, v49, v25 offset:2560
	ds_read_b32 v66, v49 offset:3328
	s_mov_b64 exec, s[70:71]
.Lcsk_14:
	v_bfe_u32 v49, v32, 16, 7
	v_cndmask_b32_e64 v49, v49, v24, s[38:39]
	v_lshlrev_b32_e32 v49, 2, v49
	s_waitcnt vmcnt(7)
	s_andn2_b64 s[68:69], exec, s[38:39]
	s_cbranch_scc0 .Lcsk_15
	s_mov_b64 s[70:71], exec
	s_mov_b64 exec, s[68:69]
	ds_add_u32 v49, v106 offset:1024
	ds_add_u32 v49, v107 offset:1792
	ds_add_rtn_u32 v63, v49, v25 offset:2560
	ds_read_b32 v64, v49 offset:3328
	s_mov_b64 exec, s[70:71]
.Lcsk_15:
	v_bfe_u32 v49, v31, 16, 7
	v_cndmask_b32_e64 v49, v49, v24, s[36:37]
	v_lshlrev_b32_e32 v49, 2, v49
	s_waitcnt vmcnt(6)
	s_andn2_b64 s[68:69], exec, s[36:37]
	s_cbranch_scc0 .Lcsk_16
	s_mov_b64 s[70:71], exec
	s_mov_b64 exec, s[68:69]
	ds_add_u32 v49, v108 offset:1024
	ds_add_u32 v49, v109 offset:1792
	ds_add_rtn_u32 v61, v49, v25 offset:2560
	ds_read_b32 v62, v49 offset:3328
	s_mov_b64 exec, s[70:71]
.Lcsk_16:
	v_bfe_u32 v49, v30, 16, 7
	v_cndmask_b32_e64 v49, v49, v24, s[34:35]
	v_lshlrev_b32_e32 v49, 2, v49
	s_waitcnt vmcnt(5)
	s_andn2_b64 s[68:69], exec, s[34:35]
	s_cbranch_scc0 .Lcsk_17
	s_mov_b64 s[70:71], exec
	s_mov_b64 exec, s[68:69]
	ds_add_u32 v49, v110 offset:1024
	ds_add_u32 v49, v111 offset:1792
	ds_add_rtn_u32 v59, v49, v25 offset:2560
	ds_read_b32 v60, v49 offset:3328
	s_mov_b64 exec, s[70:71]
.Lcsk_17:
	v_bfe_u32 v49, v29, 16, 7
	v_cndmask_b32_e64 v49, v49, v24, s[30:31]
	v_lshlrev_b32_e32 v49, 2, v49
	s_waitcnt vmcnt(4)
	s_andn2_b64 s[68:69], exec, s[30:31]
	s_cbranch_scc0 .Lcsk_18
	s_mov_b64 s[70:71], exec
	s_mov_b64 exec, s[68:69]
	ds_add_u32 v49, v112 offset:1024
	ds_add_u32 v49, v113 offset:1792
	ds_add_rtn_u32 v57, v49, v25 offset:2560
	ds_read_b32 v58, v49 offset:3328
	s_mov_b64 exec, s[70:71]
.Lcsk_18:
	v_bfe_u32 v49, v28, 16, 7
	v_cndmask_b32_e64 v49, v49, v24, s[28:29]
	v_lshlrev_b32_e32 v49, 2, v49
	s_waitcnt vmcnt(3)
	s_andn2_b64 s[68:69], exec, s[28:29]
	s_cbranch_scc0 .Lcsk_19
	s_mov_b64 s[70:71], exec
	s_mov_b64 exec, s[68:69]
	ds_add_u32 v49, v114 offset:1024
	ds_add_u32 v49, v115 offset:1792
	ds_add_rtn_u32 v54, v49, v25 offset:2560
	ds_read_b32 v56, v49 offset:3328
	s_mov_b64 exec, s[70:71]
.Lcsk_19:
	v_bfe_u32 v49, v27, 16, 7
	v_cndmask_b32_e64 v49, v49, v24, s[26:27]
	v_lshlrev_b32_e32 v49, 2, v49
	s_waitcnt vmcnt(2)
	s_andn2_b64 s[68:69], exec, s[26:27]
	s_cbranch_scc0 .Lcsk_20
	s_mov_b64 s[70:71], exec
	s_mov_b64 exec, s[68:69]
	ds_add_u32 v49, v116 offset:1024
	ds_add_u32 v49, v117 offset:1792
	ds_add_rtn_u32 v51, v49, v25 offset:2560
	ds_read_b32 v52, v49 offset:3328
	s_mov_b64 exec, s[70:71]
.Lcsk_20:
	v_bfe_u32 v49, v26, 16, 7
	v_cndmask_b32_e64 v49, v49, v24, s[24:25]
	v_bfe_u32 v53, v2, 16, 7
	v_lshlrev_b32_e32 v50, 2, v49
	v_cndmask_b32_e64 v53, v53, v24, s[22:23]
	s_waitcnt vmcnt(1)
	s_andn2_b64 s[68:69], exec, s[24:25]
	s_cbranch_scc0 .Lcsk_21
	s_mov_b64 s[70:71], exec
	s_mov_b64 exec, s[68:69]
	ds_add_u32 v50, v118 offset:1024
	ds_add_u32 v50, v119 offset:1792
	ds_add_rtn_u32 v49, v50, v25 offset:2560
	s_mov_b64 exec, s[70:71]
.Lcsk_21:
	v_lshlrev_b32_e32 v55, 2, v53
	s_andn2_b64 s[68:69], exec, s[24:25]
	s_cbranch_scc0 .Lcsk_22
	s_mov_b64 s[70:71], exec
	s_mov_b64 exec, s[68:69]
	ds_read_b32 v50, v50 offset:3328
	s_mov_b64 exec, s[70:71]
.Lcsk_22:
	s_waitcnt vmcnt(0)
	s_andn2_b64 s[68:69], exec, s[22:23]
	s_cbranch_scc0 .Lcsk_23
	s_mov_b64 s[70:71], exec
	s_mov_b64 exec, s[68:69]
	ds_add_u32 v55, v120 offset:1024
	ds_add_u32 v55, v121 offset:1792
	ds_add_rtn_u32 v53, v55, v25 offset:2560
	ds_read_b32 v55, v55 offset:3328
	s_mov_b64 exec, s[70:71]

	.amdhsa_kernel _Z5k_csrPKjS0_PK15HIP_vector_typeIiLj2EEPKiPiPjPS1_IfLj2EE
		.amdhsa_group_segment_fixed_size 4128
		.amdhsa_private_segment_fixed_size 0
		.amdhsa_kernarg_size 56
		.amdhsa_user_sgpr_count 2
		.amdhsa_user_sgpr_dispatch_ptr 0
		.amdhsa_user_sgpr_queue_ptr 0
		.amdhsa_user_sgpr_kernarg_segment_ptr 1
		.amdhsa_user_sgpr_dispatch_id 0
		.amdhsa_user_sgpr_kernarg_preload_length 0
		.amdhsa_user_sgpr_kernarg_preload_offset 0
		.amdhsa_user_sgpr_private_segment_size 0
		.amdhsa_uses_dynamic_stack 0
		.amdhsa_enable_private_segment 0
		.amdhsa_system_sgpr_workgroup_id_x 1
		.amdhsa_system_sgpr_workgroup_id_y 0
		.amdhsa_system_sgpr_workgroup_id_z 0
		.amdhsa_system_sgpr_workgroup_info 0
		.amdhsa_system_vgpr_workitem_id 0
		.amdhsa_next_free_vgpr 126
		.amdhsa_next_free_sgpr 72
		.amdhsa_accum_offset 128
		.amdhsa_reserve_vcc 1
		.amdhsa_float_round_mode_32 0
		.amdhsa_float_round_mode_16_64 0
		.amdhsa_float_denorm_mode_32 3
		.amdhsa_float_denorm_mode_16_64 3
		.amdhsa_dx10_clamp 1
		.amdhsa_ieee_mode 1
		.amdhsa_fp16_overflow 0
		.amdhsa_tg_split 0
		.amdhsa_exception_fp_ieee_invalid_op 0
		.amdhsa_exception_fp_denorm_src 0
		.amdhsa_exception_fp_ieee_div_zero 0
		.amdhsa_exception_fp_ieee_overflow 0
		.amdhsa_exception_fp_ieee_underflow 0
		.amdhsa_exception_fp_ieee_inexact 0
		.amdhsa_exception_int_div_zero 0
	.end_amdhsa_kernel

amdhsa.kernels:
  - .agpr_count:     0
    .args:
      - .actual_access:  read_only
        .address_space:  global
        .offset:         0
        .size:           8
        .value_kind:     global_buffer
      - .actual_access:  read_only
        .address_space:  global
        .offset:         8
        .size:           8
        .value_kind:     global_buffer
      - .actual_access:  write_only
        .address_space:  global
        .offset:         16
        .size:           8
        .value_kind:     global_buffer
      - .actual_access:  write_only
        .address_space:  global
        .offset:         24
        .size:           8
        .value_kind:     global_buffer
      - .actual_access:  write_only
        .address_space:  global
        .offset:         32
        .size:           8
        .value_kind:     global_buffer
      - .actual_access:  write_only
        .address_space:  global
        .offset:         40
        .size:           8
        .value_kind:     global_buffer
      - .actual_access:  write_only
        .address_space:  global
        .offset:         48
        .size:           8
        .value_kind:     global_buffer
      - .actual_access:  write_only
        .address_space:  global
        .offset:         56
        .size:           8
        .value_kind:     global_buffer
      - .actual_access:  read_only
        .address_space:  global
        .offset:         64
        .size:           8
        .value_kind:     global_buffer
      - .actual_access:  write_only
        .address_space:  global
        .offset:         72
        .size:           8
        .value_kind:     global_buffer
    .group_segment_fixed_size: 18800
    .kernarg_segment_align: 8
    .kernarg_segment_size: 80
    .language:       OpenCL C
    .language_version:
      - 2
      - 0
    .max_flat_workgroup_size: 1024
    .name:           _Z6k_partPKiS0_PjPhS1_S1_PfS3_PKfPDF16_
    .private_segment_fixed_size: 0
    .sgpr_count:     48
    .sgpr_spill_count: 0
    .symbol:         _Z6k_partPKiS0_PjPhS1_S1_PfS3_PKfPDF16_.kd
    .uniform_work_group_size: 1
    .uses_dynamic_stack: false
    .vgpr_count:     40
    .vgpr_spill_count: 0
    .wavefront_size: 64
  - .agpr_count:     0
    .args:
      - .actual_access:  read_only
        .address_space:  global
        .offset:         0
        .size:           8
        .value_kind:     global_buffer
      - .actual_access:  read_only
        .address_space:  global
        .offset:         8
        .size:           8
        .value_kind:     global_buffer
      - .actual_access:  read_only
        .address_space:  global
        .offset:         16
        .size:           8
        .value_kind:     global_buffer
      - .actual_access:  read_only
        .address_space:  global
        .offset:         24
        .size:           8
        .value_kind:     global_buffer
      - .actual_access:  write_only
        .address_space:  global
        .offset:         32
        .size:           8
        .value_kind:     global_buffer
      - .actual_access:  write_only
        .address_space:  global
        .offset:         40
        .size:           8
        .value_kind:     global_buffer
    .group_segment_fixed_size: 3076
    .kernarg_segment_align: 8
    .kernarg_segment_size: 48
    .language:       OpenCL C
    .language_version:
      - 2
      - 0
    .max_flat_workgroup_size: 512
    .name:           _Z5k_degPKjPKhS0_S0_P15HIP_vector_typeIiLj2EEPi
    .private_segment_fixed_size: 0
    .sgpr_count:     74
    .sgpr_spill_count: 0
    .symbol:         _Z5k_degPKjPKhS0_S0_P15HIP_vector_typeIiLj2EEPi.kd
    .uniform_work_group_size: 1
    .uses_dynamic_stack: false
    .vgpr_count:     61
    .vgpr_spill_count: 0
    .wavefront_size: 64
  - .agpr_count:     0
    .args:
      - .actual_access:  read_only
        .address_space:  global
        .offset:         0
        .size:           8
        .value_kind:     global_buffer
      - .actual_access:  read_only
        .address_space:  global
        .offset:         8
        .size:           8
        .value_kind:     global_buffer
      - .actual_access:  read_only
        .address_space:  global
        .offset:         16
        .size:           8
        .value_kind:     global_buffer
      - .actual_access:  read_only
        .address_space:  global
        .offset:         24
        .size:           8
        .value_kind:     global_buffer
      - .actual_access:  write_only
        .address_space:  global
        .offset:         32
        .size:           8
        .value_kind:     global_buffer
      - .actual_access:  write_only
        .address_space:  global
        .offset:         40
        .size:           8
        .value_kind:     global_buffer
      - .actual_access:  write_only
        .address_space:  global
        .offset:         48
        .size:           8
        .value_kind:     global_buffer
    .group_segment_fixed_size: 4128
    .kernarg_segment_align: 8
    .kernarg_segment_size: 56
    .language:       OpenCL C
    .language_version:
      - 2
      - 0
    .max_flat_workgroup_size: 256
    .name:           _Z5k_csrPKjS0_PK15HIP_vector_typeIiLj2EEPKiPiPjPS1_IfLj2EE
    .private_segment_fixed_size: 0
    .sgpr_count:     78
    .sgpr_spill_count: 0
    .symbol:         _Z5k_csrPKjS0_PK15HIP_vector_typeIiLj2EEPKiPiPjPS1_IfLj2EE.kd
    .uniform_work_group_size: 1
    .uses_dynamic_stack: false
    .vgpr_count:     126
    .vgpr_spill_count: 0
    .wavefront_size: 64
  - .agpr_count:     0
    .args:
      - .actual_access:  read_only
        .address_space:  global
        .offset:         0
        .size:           8
        .value_kind:     global_buffer
      - .actual_access:  read_only
        .address_space:  global
        .offset:         8
        .size:           8
        .value_kind:     global_buffer
      - .actual_access:  read_only
        .address_space:  global
        .offset:         16
        .size:           8
        .value_kind:     global_buffer
      - .actual_access:  read_only
        .address_space:  global
        .offset:         24
        .size:           8
        .value_kind:     global_buffer
      - .actual_access:  read_only
        .address_space:  global
        .offset:         32
        .size:           8
        .value_kind:     global_buffer
      - .actual_access:  read_only
        .address_space:  global
        .offset:         40
        .size:           8
        .value_kind:     global_buffer
      - .actual_access:  read_only
        .address_space:  global
        .offset:         48
        .size:           8
        .value_kind:     global_buffer
      - .address_space:  global
        .offset:         56
        .size:           8
        .value_kind:     global_buffer
    .group_segment_fixed_size: 151664
    .kernarg_segment_align: 8
    .kernarg_segment_size: 64
    .language:       OpenCL C
    .language_version:
      - 2
      - 0
    .max_flat_workgroup_size: 1024
    .name:           _Z6k_mainPKiPKjPK15HIP_vector_typeIfLj2EEPKfS8_PKDF16_S8_Pf
    .private_segment_fixed_size: 0
    .sgpr_count:     84
    .sgpr_spill_count: 0
    .symbol:         _Z6k_mainPKiPKjPK15HIP_vector_typeIfLj2EEPKfS8_PKDF16_S8_Pf.kd
    .uniform_work_group_size: 1
    .uses_dynamic_stack: false
    .vgpr_count:     128
    .vgpr_spill_count: 0
    .wavefront_size: 64
  - .agpr_count:     0
    .args:
      - .actual_access:  read_only
        .address_space:  global
        .offset:         0
        .size:           8
        .value_kind:     global_buffer
      - .actual_access:  read_only
        .address_space:  global
        .offset:         8
        .size:           8
        .value_kind:     global_buffer
      - .actual_access:  read_only
        .address_space:  global
        .offset:         16
        .size:           8
        .value_kind:     global_buffer
      - .actual_access:  read_only
        .address_space:  global
        .offset:         24
        .size:           8
        .value_kind:     global_buffer
      - .actual_access:  read_only
        .address_space:  global
        .offset:         32
        .size:           8
        .value_kind:     global_buffer
      - .actual_access:  read_only
        .address_space:  global
        .offset:         40
        .size:           8
        .value_kind:     global_buffer
      - .actual_access:  read_only
        .address_space:  global
        .offset:         48
        .size:           8
        .value_kind:     global_buffer
      - .actual_access:  read_only
        .address_space:  global
        .offset:         56
        .size:           8
        .value_kind:     global_buffer
      - .actual_access:  read_only
        .address_space:  global
        .offset:         64
        .size:           8
        .value_kind:     global_buffer
      - .actual_access:  read_only
        .address_space:  global
        .offset:         72
        .size:           8
        .value_kind:     global_buffer
      - .address_space:  global
        .offset:         80
        .size:           8
        .value_kind:     global_buffer
    .group_segment_fixed_size: 2688
    .kernarg_segment_align: 8
    .kernarg_segment_size: 88
    .language:       OpenCL C
    .language_version:
      - 2
      - 0
    .max_flat_workgroup_size: 256
    .name:           _Z7k_finalPKfS0_S0_S0_S0_S0_S0_S0_S0_S0_Pf
    .private_segment_fixed_size: 0
    .sgpr_count:     54
    .sgpr_spill_count: 0
    .symbol:         _Z7k_finalPKfS0_S0_S0_S0_S0_S0_S0_S0_S0_Pf.kd
    .uniform_work_group_size: 1
    .uses_dynamic_stack: false
    .vgpr_count:     256
    .vgpr_spill_count: 0
    .wavefront_size: 64
